# v030 + one static priority raise for wave 0 in the mLSTM scan loop (it carries the per-step scalar block), reset at loop exit
# baseline (speedup 1.0000x reference)
.LBB0_392:
	s_setprio 0
	s_nop 0
	v_readlane_b32 s0, v255, 5
	s_add_i32 s44, s44, s0
	v_readlane_b32 s46, v255, 43
	v_readlane_b32 s0, v255, 21
	s_add_i32 s46, s46, s0
	v_readlane_b32 s51, v255, 42
	v_readlane_b32 s0, v255, 22
	s_add_i32 s51, s51, s0
	v_readlane_b32 s16, v255, 30
	s_cmpk_gt_i32 s44, 0xff
	v_readlane_b32 s17, v255, 31
	s_waitcnt lgkmcnt(0)
	s_barrier
	s_cbranch_scc1 .LBB0_469

.LBB0_451:
	s_or_b64 exec, exec, s[28:29]
	v_readlane_b32 s28, v255, 13
	v_readlane_b32 s29, v255, 14
	s_or_b64 s[28:29], s[28:29], s[88:89]
	s_and_b64 vcc, exec, s[28:29]
	s_setprio 1
	s_nop 0
	s_cbranch_vccnz .LBB0_455
	s_waitcnt vmcnt(16)
	s_mov_b32 s7, 0xbfb8aa3b
	v_mul_f32_e64 v94, |v237|, s7
	v_exp_f32_e32 v94, v94
	s_mov_b32 s28, 0x800000
	v_mov_b32_e32 v97, 0xff800000
	s_bitcmp1_b32 s10, 0
	v_add_f32_e32 v94, 1.0, v94
	v_cmp_gt_f32_e32 vcc, s28, v94
	s_mov_b32 s28, 0x3f317217
	s_cselect_b32 s7, 0x520, 0
	v_cndmask_b32_e64 v95, 0, 32, vcc
	v_ldexp_f32 v94, v94, v95
	v_log_f32_e32 v94, v94
	v_max_f32_e32 v95, v237, v237
	v_min_f32_e32 v95, 0, v95
	s_add_i32 s7, s7, 0
	v_mul_f32_e32 v96, 0x3f317217, v94
	v_fma_f32 v96, v94, s28, -v96
	v_fmac_f32_e32 v96, 0x3377d1cf, v94
	s_mov_b32 s28, 0x7f800000
	v_fmac_f32_e32 v96, 0x3f317217, v94
	v_cmp_lt_f32_e64 s[28:29], |v94|, s28
	s_add_i32 s7, s7, 0x1e040
	v_readlane_b32 s60, v255, 36
	v_cndmask_b32_e64 v94, v94, v96, s[28:29]
	v_cndmask_b32_e32 v96, 0, v120, vcc
	v_sub_f32_e32 v94, v94, v96
	v_sub_f32_e32 v94, v95, v94
	v_mov_b32_e32 v95, v107
	v_mov_b32_e32 v96, 0xff800000
	v_add_f32_dpp v94, v94, v94 row_shr:1 row_mask:0xf bank_mask:0xf bound_ctrl:1
	v_lshl_add_u32 v99, v123, 2, s7
	v_readlane_b32 s61, v255, 37
	v_add_f32_dpp v94, v94, v94 row_shr:2 row_mask:0xf bank_mask:0xf bound_ctrl:1
	s_nop 1
	v_add_f32_dpp v94, v94, v94 row_shr:4 row_mask:0xf bank_mask:0xf bound_ctrl:1
	s_nop 1
	v_add_f32_dpp v94, v94, v94 row_shr:8 row_mask:0xf bank_mask:0xf bound_ctrl:1
	s_nop 1
	v_mov_b32_dpp v95, v94 row_bcast:15 row_mask:0xa bank_mask:0xf
	v_add_f32_e32 v94, v94, v95
	v_mov_b32_e32 v95, v107
	s_nop 1
	v_mov_b32_dpp v95, v94 row_bcast:31 row_mask:0xc bank_mask:0xf
	v_add_f32_e32 v94, v94, v95
	v_sub_f32_e32 v95, v236, v94
	v_readlane_b32 s31, v94, 63
	s_nop 0
	v_mov_b32_dpp v96, v95 row_shr:1 row_mask:0xf bank_mask:0xf
	v_max_f32_e32 v96, v96, v96
	v_max_f32_e32 v96, v95, v96
	s_nop 1
	v_mov_b32_dpp v97, v96 row_shr:2 row_mask:0xf bank_mask:0xf
	v_max_f32_e32 v97, v97, v97
	v_max_f32_e32 v96, v96, v97
	v_mov_b32_e32 v97, 0xff800000
	s_nop 1
	v_mov_b32_dpp v97, v96 row_shr:4 row_mask:0xf bank_mask:0xf
	v_max_f32_e32 v97, v97, v97
	v_max_f32_e32 v96, v96, v97
	v_mov_b32_e32 v97, 0xff800000
	s_nop 1
	v_mov_b32_dpp v97, v96 row_shr:8 row_mask:0xf bank_mask:0xf
	v_max_f32_e32 v97, v97, v97
	v_max_f32_e32 v96, v96, v97
	v_mov_b32_e32 v97, 0xff800000
	s_nop 1
	v_mov_b32_dpp v97, v96 row_bcast:15 row_mask:0xa bank_mask:0xf
	v_max_f32_e32 v97, v97, v97
	v_max_f32_e32 v96, v96, v97
	v_mov_b32_e32 v97, 0xff800000
	s_nop 1
	v_mov_b32_dpp v97, v96 row_bcast:31 row_mask:0xc bank_mask:0xf
	v_max3_f32 v96, v127, v96, v97
	v_sub_f32_e32 v97, v127, v96
	v_readlane_b32 s30, v96, 63
	v_sub_f32_e64 v94, -v94, v96
	v_mul_f32_e32 v97, 0x3fb8aa3b, v97
	v_mul_f32_e32 v94, 0x3fb8aa3b, v94
	v_subrev_f32_e32 v98, s30, v95
	v_exp_f32_e32 v97, v97
	v_exp_f32_e32 v94, v94
	v_mul_f32_e32 v98, 0x3fb8aa3b, v98
	v_exp_f32_e32 v98, v98
	ds_write2st64_b32 v99, v95, v96 offset1:1
	ds_write2st64_b32 v99, v97, v94 offset0:2 offset1:3
	ds_write_b32 v99, v98 offset:1024
	s_and_saveexec_b64 s[28:29], s[60:61]
	s_cbranch_execz .LBB0_454
	v_subrev_f32_e32 v94, s30, v127
	v_mul_f32_e32 v94, 0x3fb8aa3b, v94
	v_exp_f32_e32 v94, v94
	v_mov_b32_e32 v95, s7
	ds_write_b32 v95, v94 offset:1280
